# moe_tables: serial one-lane per-expert table loop replaced by a 32-lane version (scalar running prefix via readlane/writelane, every lane writes its own expert's tiles); same tables
# speedup vs baseline: 1.0155x; 1.0085x over previous
; #define LDS_WAIT() asm volatile("s_waitcnt lgkmcnt(0)" ::: "memory")
; __device__ __forceinline__ void moe_tables(Frame& F, int l) {
;     __syncthreads();
;     if (F.wave == 0) {
;         if (F.lane < NE) F.MISC[MT_CNT + F.lane] = __hip_atomic_load(F.ctl + CW_CNT + l * 2048 + F.lane * 64, RLX_AGENT);
;         LDS_WAIT();
;         if (F.lane == 0) { int g = 0;
;             for (int e = 0; e < NE; ++e) { const int n = (int)F.MISC[MT_CNT + e];
;                 if (blockIdx.x == 0) __hip_atomic_store(F.ctl + CW_TB + l * 64 + e, (unsigned)(g * 256), RLX_AGENT);
;                 const int nt = (n + 255) >> 8; for (int r = 0; r < nt && g < 96; ++r, ++g) { F.MISC[MT_TE + g] = (unsigned)e; F.MISC[MT_TR + g] = (unsigned)r; } }
;             F.MISC[MT_NT] = (unsigned)g; } }
;     LDS_WAIT(); __syncthreads();
.LBB0_1557:
	s_or_b64 exec, exec, s[4:5]
	v_cmp_gt_i32_e32 vcc, 32, v66
	s_and_saveexec_b64 s[4:5], vcc
	v_add_u32_e32 v3, 0xff, v2
	v_ashrrev_i32_e32 v3, 8, v3
	v_readlane_b32 s0, v248, 36
	v_readlane_b32 s1, v248, 37
	s_nop 3
	s_add_u32 s14, s48, s0
	s_addc_u32 s15, s49, s1
	s_add_u32 s14, s14, 0x40000
	s_addc_u32 s15, s15, 0
	v_readlane_b32 s0, v250, 41
	v_readlane_b32 s1, v250, 42
	s_mov_b32 s6, 0
	s_min_u32 s9, s6, 0x60
	v_writelane_b32 v0, s9, 0
	v_readlane_b32 s10, v3, 0
	s_add_u32 s6, s6, s10
	s_min_u32 s9, s6, 0x60
	v_writelane_b32 v0, s9, 1
	v_readlane_b32 s10, v3, 1
	s_add_u32 s6, s6, s10
	s_min_u32 s9, s6, 0x60
	v_writelane_b32 v0, s9, 2
	v_readlane_b32 s10, v3, 2
	s_add_u32 s6, s6, s10
	s_min_u32 s9, s6, 0x60
	v_writelane_b32 v0, s9, 3
	v_readlane_b32 s10, v3, 3
	s_add_u32 s6, s6, s10
	s_min_u32 s9, s6, 0x60
	v_writelane_b32 v0, s9, 4
	v_readlane_b32 s10, v3, 4
	s_add_u32 s6, s6, s10
	s_min_u32 s9, s6, 0x60
	v_writelane_b32 v0, s9, 5
	v_readlane_b32 s10, v3, 5
	s_add_u32 s6, s6, s10
	s_min_u32 s9, s6, 0x60
	v_writelane_b32 v0, s9, 6
	v_readlane_b32 s10, v3, 6
	s_add_u32 s6, s6, s10
	s_min_u32 s9, s6, 0x60
	v_writelane_b32 v0, s9, 7
	v_readlane_b32 s10, v3, 7
	s_add_u32 s6, s6, s10
	s_min_u32 s9, s6, 0x60
	v_writelane_b32 v0, s9, 8
	v_readlane_b32 s10, v3, 8
	s_add_u32 s6, s6, s10
	s_min_u32 s9, s6, 0x60
	v_writelane_b32 v0, s9, 9
	v_readlane_b32 s10, v3, 9
	s_add_u32 s6, s6, s10
	s_min_u32 s9, s6, 0x60
	v_writelane_b32 v0, s9, 10
	v_readlane_b32 s10, v3, 10
	s_add_u32 s6, s6, s10
	s_min_u32 s9, s6, 0x60
	v_writelane_b32 v0, s9, 11
	v_readlane_b32 s10, v3, 11
	s_add_u32 s6, s6, s10
	s_min_u32 s9, s6, 0x60
	v_writelane_b32 v0, s9, 12
	v_readlane_b32 s10, v3, 12
	s_add_u32 s6, s6, s10
	s_min_u32 s9, s6, 0x60
	v_writelane_b32 v0, s9, 13
	v_readlane_b32 s10, v3, 13
	s_add_u32 s6, s6, s10
	s_min_u32 s9, s6, 0x60
	v_writelane_b32 v0, s9, 14
	v_readlane_b32 s10, v3, 14
	s_add_u32 s6, s6, s10
	s_min_u32 s9, s6, 0x60
	v_writelane_b32 v0, s9, 15
	v_readlane_b32 s10, v3, 15
	s_add_u32 s6, s6, s10
	s_min_u32 s9, s6, 0x60
	v_writelane_b32 v0, s9, 16
	v_readlane_b32 s10, v3, 16
	s_add_u32 s6, s6, s10
	s_min_u32 s9, s6, 0x60
	v_writelane_b32 v0, s9, 17
	v_readlane_b32 s10, v3, 17
	s_add_u32 s6, s6, s10
	s_min_u32 s9, s6, 0x60
	v_writelane_b32 v0, s9, 18
	v_readlane_b32 s10, v3, 18
	s_add_u32 s6, s6, s10
	s_min_u32 s9, s6, 0x60
	v_writelane_b32 v0, s9, 19
	v_readlane_b32 s10, v3, 19
	s_add_u32 s6, s6, s10
	s_min_u32 s9, s6, 0x60
	v_writelane_b32 v0, s9, 20
	v_readlane_b32 s10, v3, 20
	s_add_u32 s6, s6, s10
	s_min_u32 s9, s6, 0x60
	v_writelane_b32 v0, s9, 21
	v_readlane_b32 s10, v3, 21
	s_add_u32 s6, s6, s10
	s_min_u32 s9, s6, 0x60
	v_writelane_b32 v0, s9, 22
	v_readlane_b32 s10, v3, 22
	s_add_u32 s6, s6, s10
	s_min_u32 s9, s6, 0x60
	v_writelane_b32 v0, s9, 23
	v_readlane_b32 s10, v3, 23
	s_add_u32 s6, s6, s10
	s_min_u32 s9, s6, 0x60
	v_writelane_b32 v0, s9, 24
	v_readlane_b32 s10, v3, 24
	s_add_u32 s6, s6, s10
	s_min_u32 s9, s6, 0x60
	v_writelane_b32 v0, s9, 25
	v_readlane_b32 s10, v3, 25
	s_add_u32 s6, s6, s10
	s_min_u32 s9, s6, 0x60
	v_writelane_b32 v0, s9, 26
	v_readlane_b32 s10, v3, 26
	s_add_u32 s6, s6, s10
	s_min_u32 s9, s6, 0x60
	v_writelane_b32 v0, s9, 27
	v_readlane_b32 s10, v3, 27
	s_add_u32 s6, s6, s10
	s_min_u32 s9, s6, 0x60
	v_writelane_b32 v0, s9, 28
	v_readlane_b32 s10, v3, 28
	s_add_u32 s6, s6, s10
	s_min_u32 s9, s6, 0x60
	v_writelane_b32 v0, s9, 29
	v_readlane_b32 s10, v3, 29
	s_add_u32 s6, s6, s10
	s_min_u32 s9, s6, 0x60
	v_writelane_b32 v0, s9, 30
	v_readlane_b32 s10, v3, 30
	s_add_u32 s6, s6, s10
	s_min_u32 s9, s6, 0x60
	v_writelane_b32 v0, s9, 31
	v_readlane_b32 s10, v3, 31
	s_add_u32 s6, s6, s10
	s_min_u32 s6, s6, 0x60
	s_andn2_b64 vcc, exec, s[0:1]
	s_cbranch_vccnz .Lmt_notb
	v_lshlrev_b32_e32 v5, 8, v0
	v_lshlrev_b32_e32 v6, 2, v66
	global_store_dword v6, v5, s[14:15] sc1
.Lmt_notb:
	v_mov_b32_e32 v8, 0
	v_mov_b32_e32 v9, 0x60
.Lmt_loop:
	v_cmp_lt_i32_e32 vcc, v8, v3
	v_add_u32_e32 v6, v0, v8
	v_cmp_lt_u32_e64 s[10:11], v6, v9
	s_and_b64 s[10:11], vcc, s[10:11]
	s_cbranch_scc0 .Lmt_done
	s_mov_b64 s[12:13], exec
	s_mov_b64 exec, s[10:11]
	v_lshlrev_b32_e32 v7, 2, v6
	v_add_u32_e32 v7, 0x20180, v7
	ds_write_b32 v7, v66
	ds_write_b32 v7, v8 offset:384
	s_mov_b64 exec, s[12:13]
	v_add_u32_e32 v8, 1, v8
	s_branch .Lmt_loop
.Lmt_done:
	v_readlane_b32 s0, v248, 0
	v_mov_b32_e32 v5, s6
	s_nop 1
	v_mov_b32_e32 v6, s0
	ds_write_b32 v6, v5
